# v52 plus G1/G2 K-loop counter/pointer SALU block moved in front of the loop-back barrier
# speedup vs baseline: 1.0007x; 1.0007x over previous
.LBB0_310:
	v_add_u32_e32 v64, s34, v185
	ds_read_b128 v[130:133], v64
	ds_read_b128 v[134:137], v64 offset:1024
	ds_read_b128 v[138:141], v64 offset:2048
	ds_read_b128 v[142:145], v64 offset:3072
	v_add_u32_e32 v64, s37, v185
	ds_read_b128 v[158:161], v64
	ds_read_b128 v[162:165], v64 offset:1024
	ds_read_b128 v[166:169], v64 offset:2048
	ds_read_b128 v[170:173], v64 offset:3072
	s_add_u32 s26, s24, 0xfffc0080
	s_addc_u32 s27, s25, -1
	s_cmp_eq_u32 s56, 12
	s_cselect_b32 s29, s19, s27
	s_cselect_b32 s28, s33, s26
	s_cselect_b32 s27, s17, s55
	s_cselect_b32 s26, s53, s54
	s_add_i32 m0, s40, 0xc000
	ds_read_b128 v[174:177], v188
	ds_read_b128 v[178:181], v188 offset:1024
	ds_read_b128 v[190:193], v188 offset:2048
	ds_read_b128 v[212:215], v188 offset:3072
	ds_read_b128 v[216:219], v188 offset:4096
	ds_read_b128 v[220:223], v188 offset:5120
	ds_read_b128 v[224:227], v188 offset:6144
	ds_read_b128 v[228:231], v188 offset:7168
	global_load_lds_dwordx4 v154, s[24:25]
	s_add_i32 m0, s40, 0xe000
	s_nop 0
	global_load_lds_dwordx4 v156, s[24:25]
	s_waitcnt vmcnt(8)
	s_waitcnt lgkmcnt(0)
	s_barrier
	s_waitcnt lgkmcnt(0)
	v_mfma_f32_16x16x32_bf16 v[126:129], v[130:133], v[174:177], v[126:129]
	v_mfma_f32_16x16x32_bf16 v[122:125], v[138:141], v[174:177], v[122:125]
	v_mfma_f32_16x16x32_bf16 v[118:121], v[130:133], v[190:193], v[118:121]
	v_mfma_f32_16x16x32_bf16 v[110:113], v[138:141], v[190:193], v[110:113]
	v_mfma_f32_16x16x32_bf16 v[102:105], v[130:133], v[216:219], v[102:105]
	v_mfma_f32_16x16x32_bf16 v[94:97], v[138:141], v[216:219], v[94:97]
	v_mfma_f32_16x16x32_bf16 v[86:89], v[130:133], v[224:227], v[86:89]
	v_mfma_f32_16x16x32_bf16 v[78:81], v[138:141], v[224:227], v[78:81]
	v_mfma_f32_16x16x32_bf16 v[126:129], v[134:137], v[178:181], v[126:129]
	v_mfma_f32_16x16x32_bf16 v[122:125], v[142:145], v[178:181], v[122:125]
	v_mfma_f32_16x16x32_bf16 v[118:121], v[134:137], v[212:215], v[118:121]
	v_mfma_f32_16x16x32_bf16 v[110:113], v[142:145], v[212:215], v[110:113]
	v_mfma_f32_16x16x32_bf16 v[102:105], v[134:137], v[220:223], v[102:105]
	v_mfma_f32_16x16x32_bf16 v[94:97], v[142:145], v[220:223], v[94:97]
	v_mfma_f32_16x16x32_bf16 v[86:89], v[134:137], v[228:231], v[86:89]
	v_mfma_f32_16x16x32_bf16 v[78:81], v[142:145], v[228:231], v[78:81]
	v_mfma_f32_16x16x32_bf16 v[114:117], v[158:161], v[174:177], v[114:117]
	v_mfma_f32_16x16x32_bf16 v[106:109], v[166:169], v[174:177], v[106:109]
	v_mfma_f32_16x16x32_bf16 v[98:101], v[158:161], v[190:193], v[98:101]
	v_mfma_f32_16x16x32_bf16 v[90:93], v[166:169], v[190:193], v[90:93]
	v_mfma_f32_16x16x32_bf16 v[82:85], v[158:161], v[216:219], v[82:85]
	v_mfma_f32_16x16x32_bf16 v[74:77], v[166:169], v[216:219], v[74:77]
	v_mfma_f32_16x16x32_bf16 v[70:73], v[158:161], v[224:227], v[70:73]
	v_mfma_f32_16x16x32_bf16 v[66:69], v[166:169], v[224:227], v[66:69]
	v_mfma_f32_16x16x32_bf16 v[114:117], v[162:165], v[178:181], v[114:117]
	v_mfma_f32_16x16x32_bf16 v[106:109], v[170:173], v[178:181], v[106:109]
	v_mfma_f32_16x16x32_bf16 v[98:101], v[162:165], v[212:215], v[98:101]
	v_mfma_f32_16x16x32_bf16 v[90:93], v[170:173], v[212:215], v[90:93]
	v_mfma_f32_16x16x32_bf16 v[82:85], v[162:165], v[220:223], v[82:85]
	v_mfma_f32_16x16x32_bf16 v[74:77], v[170:173], v[220:223], v[74:77]
	v_mfma_f32_16x16x32_bf16 v[70:73], v[162:165], v[228:231], v[70:73]
	v_mfma_f32_16x16x32_bf16 v[66:69], v[170:173], v[228:231], v[66:69]
	s_barrier
	s_mov_b32 m0, s35
	s_add_u32 s58, s26, 0x40000
	ds_read_b128 v[174:177], v188 offset:16384
	ds_read_b128 v[178:181], v188 offset:17408
	ds_read_b128 v[190:193], v188 offset:18432
	ds_read_b128 v[212:215], v188 offset:19456
	ds_read_b128 v[216:219], v188 offset:20480
	ds_read_b128 v[220:223], v188 offset:21504
	ds_read_b128 v[224:227], v188 offset:22528
	ds_read_b128 v[228:231], v188 offset:23552
	global_load_lds_dwordx4 v150, s[26:27]
	s_mov_b32 m0, s36
	s_addc_u32 s59, s27, 0
	global_load_lds_dwordx4 v146, s[26:27]
	s_mov_b32 m0, s38
	s_nop 0
	global_load_lds_dwordx4 v150, s[58:59]
	s_mov_b32 m0, s39
	s_nop 0
	global_load_lds_dwordx4 v146, s[58:59]
	s_mov_b32 m0, s40
	s_nop 0
	global_load_lds_dwordx4 v152, s[28:29]
	s_mov_b32 m0, s41
	s_nop 0
	global_load_lds_dwordx4 v148, s[28:29]
	s_waitcnt vmcnt(8)
	s_waitcnt lgkmcnt(0)
	s_barrier
	s_waitcnt lgkmcnt(0)
	v_mfma_f32_16x16x32_bf16 v[60:63], v[130:133], v[174:177], v[60:63]
	v_mfma_f32_16x16x32_bf16 v[56:59], v[138:141], v[174:177], v[56:59]
	v_mfma_f32_16x16x32_bf16 v[52:55], v[130:133], v[190:193], v[52:55]
	v_mfma_f32_16x16x32_bf16 v[44:47], v[138:141], v[190:193], v[44:47]
	v_mfma_f32_16x16x32_bf16 v[36:39], v[130:133], v[216:219], v[36:39]
	v_mfma_f32_16x16x32_bf16 v[28:31], v[138:141], v[216:219], v[28:31]
	v_mfma_f32_16x16x32_bf16 v[20:23], v[130:133], v[224:227], v[20:23]
	v_mfma_f32_16x16x32_bf16 v[12:15], v[138:141], v[224:227], v[12:15]
	v_mfma_f32_16x16x32_bf16 v[60:63], v[134:137], v[178:181], v[60:63]
	v_mfma_f32_16x16x32_bf16 v[56:59], v[142:145], v[178:181], v[56:59]
	v_mfma_f32_16x16x32_bf16 v[52:55], v[134:137], v[212:215], v[52:55]
	v_mfma_f32_16x16x32_bf16 v[44:47], v[142:145], v[212:215], v[44:47]
	v_mfma_f32_16x16x32_bf16 v[36:39], v[134:137], v[220:223], v[36:39]
	v_mfma_f32_16x16x32_bf16 v[28:31], v[142:145], v[220:223], v[28:31]
	v_mfma_f32_16x16x32_bf16 v[20:23], v[134:137], v[228:231], v[20:23]
	v_mfma_f32_16x16x32_bf16 v[12:15], v[142:145], v[228:231], v[12:15]
	v_mfma_f32_16x16x32_bf16 v[48:51], v[158:161], v[174:177], v[48:51]
	v_mfma_f32_16x16x32_bf16 v[40:43], v[166:169], v[174:177], v[40:43]
	v_mfma_f32_16x16x32_bf16 v[32:35], v[158:161], v[190:193], v[32:35]
	v_mfma_f32_16x16x32_bf16 v[24:27], v[166:169], v[190:193], v[24:27]
	v_mfma_f32_16x16x32_bf16 v[16:19], v[158:161], v[216:219], v[16:19]
	v_mfma_f32_16x16x32_bf16 v[8:11], v[166:169], v[216:219], v[8:11]
	v_mfma_f32_16x16x32_bf16 v[4:7], v[158:161], v[224:227], v[4:7]
	v_mfma_f32_16x16x32_bf16 v[0:3], v[166:169], v[224:227], v[0:3]
	v_mfma_f32_16x16x32_bf16 v[48:51], v[162:165], v[178:181], v[48:51]
	v_mfma_f32_16x16x32_bf16 v[40:43], v[170:173], v[178:181], v[40:43]
	v_mfma_f32_16x16x32_bf16 v[32:35], v[162:165], v[212:215], v[32:35]
	v_mfma_f32_16x16x32_bf16 v[24:27], v[170:173], v[212:215], v[24:27]
	v_mfma_f32_16x16x32_bf16 v[16:19], v[162:165], v[220:223], v[16:19]
	v_mfma_f32_16x16x32_bf16 v[8:11], v[170:173], v[220:223], v[8:11]
	v_mfma_f32_16x16x32_bf16 v[4:7], v[162:165], v[228:231], v[4:7]
	v_mfma_f32_16x16x32_bf16 v[0:3], v[170:173], v[228:231], v[0:3]
	s_barrier
	v_add_u32_e32 v64, s44, v185
	ds_read_b128 v[130:133], v64
	ds_read_b128 v[134:137], v64 offset:1024
	ds_read_b128 v[138:141], v64 offset:2048
	ds_read_b128 v[142:145], v64 offset:3072
	v_add_u32_e32 v64, s49, v185
	ds_read_b128 v[158:161], v64
	ds_read_b128 v[162:165], v64 offset:1024
	ds_read_b128 v[166:169], v64 offset:2048
	ds_read_b128 v[170:173], v64 offset:3072
	s_add_u32 s28, s28, 0x40000
	s_addc_u32 s29, s29, 0
	s_mov_b32 m0, s42
	ds_read_b128 v[174:177], v188 offset:32768
	ds_read_b128 v[178:181], v188 offset:33792
	ds_read_b128 v[190:193], v188 offset:34816
	ds_read_b128 v[212:215], v188 offset:35840
	ds_read_b128 v[216:219], v188 offset:36864
	ds_read_b128 v[220:223], v188 offset:37888
	ds_read_b128 v[224:227], v188 offset:38912
	ds_read_b128 v[228:231], v188 offset:39936
	global_load_lds_dwordx4 v152, s[28:29]
	s_mov_b32 m0, s43
	s_nop 0
	global_load_lds_dwordx4 v148, s[28:29]
	s_waitcnt vmcnt(8)
	s_waitcnt lgkmcnt(0)
	s_barrier
	s_waitcnt lgkmcnt(0)
	v_mfma_f32_16x16x32_bf16 v[126:129], v[130:133], v[174:177], v[126:129]
	v_mfma_f32_16x16x32_bf16 v[122:125], v[138:141], v[174:177], v[122:125]
	v_mfma_f32_16x16x32_bf16 v[118:121], v[130:133], v[190:193], v[118:121]
	v_mfma_f32_16x16x32_bf16 v[110:113], v[138:141], v[190:193], v[110:113]
	v_mfma_f32_16x16x32_bf16 v[102:105], v[130:133], v[216:219], v[102:105]
	v_mfma_f32_16x16x32_bf16 v[94:97], v[138:141], v[216:219], v[94:97]
	v_mfma_f32_16x16x32_bf16 v[86:89], v[130:133], v[224:227], v[86:89]
	v_mfma_f32_16x16x32_bf16 v[78:81], v[138:141], v[224:227], v[78:81]
	v_mfma_f32_16x16x32_bf16 v[126:129], v[134:137], v[178:181], v[126:129]
	v_mfma_f32_16x16x32_bf16 v[122:125], v[142:145], v[178:181], v[122:125]
	v_mfma_f32_16x16x32_bf16 v[118:121], v[134:137], v[212:215], v[118:121]
	v_mfma_f32_16x16x32_bf16 v[110:113], v[142:145], v[212:215], v[110:113]
	v_mfma_f32_16x16x32_bf16 v[102:105], v[134:137], v[220:223], v[102:105]
	v_mfma_f32_16x16x32_bf16 v[94:97], v[142:145], v[220:223], v[94:97]
	v_mfma_f32_16x16x32_bf16 v[86:89], v[134:137], v[228:231], v[86:89]
	v_mfma_f32_16x16x32_bf16 v[78:81], v[142:145], v[228:231], v[78:81]
	v_mfma_f32_16x16x32_bf16 v[114:117], v[158:161], v[174:177], v[114:117]
	v_mfma_f32_16x16x32_bf16 v[106:109], v[166:169], v[174:177], v[106:109]
	v_mfma_f32_16x16x32_bf16 v[98:101], v[158:161], v[190:193], v[98:101]
	v_mfma_f32_16x16x32_bf16 v[90:93], v[166:169], v[190:193], v[90:93]
	v_mfma_f32_16x16x32_bf16 v[82:85], v[158:161], v[216:219], v[82:85]
	v_mfma_f32_16x16x32_bf16 v[74:77], v[166:169], v[216:219], v[74:77]
	v_mfma_f32_16x16x32_bf16 v[70:73], v[158:161], v[224:227], v[70:73]
	v_mfma_f32_16x16x32_bf16 v[66:69], v[166:169], v[224:227], v[66:69]
	v_mfma_f32_16x16x32_bf16 v[114:117], v[162:165], v[178:181], v[114:117]
	v_mfma_f32_16x16x32_bf16 v[106:109], v[170:173], v[178:181], v[106:109]
	v_mfma_f32_16x16x32_bf16 v[98:101], v[162:165], v[212:215], v[98:101]
	v_mfma_f32_16x16x32_bf16 v[90:93], v[170:173], v[212:215], v[90:93]
	v_mfma_f32_16x16x32_bf16 v[82:85], v[162:165], v[220:223], v[82:85]
	v_mfma_f32_16x16x32_bf16 v[74:77], v[170:173], v[220:223], v[74:77]
	v_mfma_f32_16x16x32_bf16 v[70:73], v[162:165], v[228:231], v[70:73]
	v_mfma_f32_16x16x32_bf16 v[66:69], v[170:173], v[228:231], v[66:69]
	s_barrier
	s_mov_b32 m0, s45
	s_add_u32 s100, s26, s68
	s_addc_u32 s101, s27, s69
	s_add_u32 s26, s26, 0x40080
	ds_read_b128 v[174:177], v188 offset:49152
	ds_read_b128 v[178:181], v188 offset:50176
	ds_read_b128 v[190:193], v188 offset:51200
	ds_read_b128 v[212:215], v188 offset:52224
	ds_read_b128 v[216:219], v188 offset:53248
	ds_read_b128 v[220:223], v188 offset:54272
	ds_read_b128 v[224:227], v188 offset:55296
	ds_read_b128 v[228:231], v188 offset:56320
	global_load_lds_dwordx4 v150, s[100:101]
	s_mov_b32 m0, s46
	s_addc_u32 s27, s27, 0
	global_load_lds_dwordx4 v146, s[100:101]
	s_mov_b32 m0, s50
	s_add_u32 s100, s28, s68
	global_load_lds_dwordx4 v150, s[26:27]
	s_addc_u32 s101, s29, s69
	s_mov_b32 m0, s51
	s_sub_u32 s100, s100, 0x40000
	global_load_lds_dwordx4 v146, s[26:27]
	s_subb_u32 s101, s101, 0
	s_mov_b32 m0, s47
	s_nop 0
	global_load_lds_dwordx4 v152, s[100:101]
	s_mov_b32 m0, s48
	s_nop 0
	global_load_lds_dwordx4 v148, s[100:101]
	s_waitcnt vmcnt(8)
	s_waitcnt lgkmcnt(0)
	s_barrier
	s_waitcnt lgkmcnt(0)
	v_mfma_f32_16x16x32_bf16 v[60:63], v[130:133], v[174:177], v[60:63]
	v_mfma_f32_16x16x32_bf16 v[56:59], v[138:141], v[174:177], v[56:59]
	v_mfma_f32_16x16x32_bf16 v[52:55], v[130:133], v[190:193], v[52:55]
	v_mfma_f32_16x16x32_bf16 v[44:47], v[138:141], v[190:193], v[44:47]
	v_mfma_f32_16x16x32_bf16 v[36:39], v[130:133], v[216:219], v[36:39]
	v_mfma_f32_16x16x32_bf16 v[28:31], v[138:141], v[216:219], v[28:31]
	v_mfma_f32_16x16x32_bf16 v[20:23], v[130:133], v[224:227], v[20:23]
	v_mfma_f32_16x16x32_bf16 v[12:15], v[138:141], v[224:227], v[12:15]
	v_mfma_f32_16x16x32_bf16 v[60:63], v[134:137], v[178:181], v[60:63]
	v_mfma_f32_16x16x32_bf16 v[56:59], v[142:145], v[178:181], v[56:59]
	v_mfma_f32_16x16x32_bf16 v[52:55], v[134:137], v[212:215], v[52:55]
	v_mfma_f32_16x16x32_bf16 v[44:47], v[142:145], v[212:215], v[44:47]
	v_mfma_f32_16x16x32_bf16 v[36:39], v[134:137], v[220:223], v[36:39]
	v_mfma_f32_16x16x32_bf16 v[28:31], v[142:145], v[220:223], v[28:31]
	v_mfma_f32_16x16x32_bf16 v[20:23], v[134:137], v[228:231], v[20:23]
	v_mfma_f32_16x16x32_bf16 v[12:15], v[142:145], v[228:231], v[12:15]
	v_mfma_f32_16x16x32_bf16 v[48:51], v[158:161], v[174:177], v[48:51]
	v_mfma_f32_16x16x32_bf16 v[40:43], v[166:169], v[174:177], v[40:43]
	v_mfma_f32_16x16x32_bf16 v[32:35], v[158:161], v[190:193], v[32:35]
	v_mfma_f32_16x16x32_bf16 v[24:27], v[166:169], v[190:193], v[24:27]
	v_mfma_f32_16x16x32_bf16 v[16:19], v[158:161], v[216:219], v[16:19]
	v_mfma_f32_16x16x32_bf16 v[8:11], v[166:169], v[216:219], v[8:11]
	v_mfma_f32_16x16x32_bf16 v[4:7], v[158:161], v[224:227], v[4:7]
	v_mfma_f32_16x16x32_bf16 v[0:3], v[166:169], v[224:227], v[0:3]
	v_mfma_f32_16x16x32_bf16 v[48:51], v[162:165], v[178:181], v[48:51]
	v_mfma_f32_16x16x32_bf16 v[40:43], v[170:173], v[178:181], v[40:43]
	v_mfma_f32_16x16x32_bf16 v[32:35], v[162:165], v[212:215], v[32:35]
	v_mfma_f32_16x16x32_bf16 v[24:27], v[170:173], v[212:215], v[24:27]
	v_mfma_f32_16x16x32_bf16 v[16:19], v[162:165], v[220:223], v[16:19]
	v_mfma_f32_16x16x32_bf16 v[8:11], v[170:173], v[220:223], v[8:11]
	v_mfma_f32_16x16x32_bf16 v[4:7], v[162:165], v[228:231], v[4:7]
	v_mfma_f32_16x16x32_bf16 v[0:3], v[170:173], v[228:231], v[0:3]
	s_add_i32 s56, s56, 2
	s_add_u32 s24, s24, 0x100
	s_addc_u32 s25, s25, 0
	s_add_u32 s54, s54, 0x100
	s_addc_u32 s55, s55, 0
	s_cmp_gt_u32 s56, 13
	s_barrier
	s_cbranch_scc0 .LBB0_310
	s_and_b64 vcc, exec, s[14:15]
	s_cbranch_vccz .LBB0_313
	s_barrier

.LBB0_814:
	v_add_u32_e32 v64, s11, v173
	ds_read_b128 v[66:69], v64
	ds_read_b128 v[70:73], v64 offset:1024
	ds_read_b128 v[74:77], v64 offset:2048
	ds_read_b128 v[78:81], v64 offset:3072
	v_add_u32_e32 v64, s34, v173
	ds_read_b128 v[146:149], v64
	ds_read_b128 v[150:153], v64 offset:1024
	ds_read_b128 v[166:169], v64 offset:2048
	ds_read_b128 v[176:179], v64 offset:3072
	s_add_u32 s4, s0, 0xfffc0080
	s_addc_u32 s5, s1, -1
	s_cmp_eq_u32 s61, 12
	s_cselect_b32 s27, s55, s5
	s_cselect_b32 s26, s56, s4
	s_cselect_b32 s5, s57, s60
	s_cselect_b32 s4, s58, s59
	s_add_i32 m0, s37, 0xc000
	ds_read_b128 v[180:183], v175
	ds_read_b128 v[184:187], v175 offset:1024
	ds_read_b128 v[188:191], v175 offset:2048
	ds_read_b128 v[192:195], v175 offset:3072
	ds_read_b128 v[212:215], v175 offset:4096
	ds_read_b128 v[216:219], v175 offset:5120
	ds_read_b128 v[220:223], v175 offset:6144
	ds_read_b128 v[224:227], v175 offset:7168
	global_load_lds_dwordx4 v162, s[0:1]
	s_add_i32 m0, s37, 0xe000
	s_nop 0
	global_load_lds_dwordx4 v164, s[0:1]
	s_waitcnt vmcnt(8)
	s_waitcnt lgkmcnt(0)
	s_barrier
	s_waitcnt lgkmcnt(0)
	v_mfma_f32_16x16x32_bf16 v[142:145], v[66:69], v[180:183], v[142:145]
	v_mfma_f32_16x16x32_bf16 v[138:141], v[74:77], v[180:183], v[138:141]
	v_mfma_f32_16x16x32_bf16 v[126:129], v[66:69], v[188:191], v[126:129]
	v_mfma_f32_16x16x32_bf16 v[122:125], v[74:77], v[188:191], v[122:125]
	v_mfma_f32_16x16x32_bf16 v[110:113], v[66:69], v[212:215], v[110:113]
	v_mfma_f32_16x16x32_bf16 v[106:109], v[74:77], v[212:215], v[106:109]
	v_mfma_f32_16x16x32_bf16 v[94:97], v[66:69], v[220:223], v[94:97]
	v_mfma_f32_16x16x32_bf16 v[90:93], v[74:77], v[220:223], v[90:93]
	v_mfma_f32_16x16x32_bf16 v[142:145], v[70:73], v[184:187], v[142:145]
	v_mfma_f32_16x16x32_bf16 v[138:141], v[78:81], v[184:187], v[138:141]
	v_mfma_f32_16x16x32_bf16 v[126:129], v[70:73], v[192:195], v[126:129]
	v_mfma_f32_16x16x32_bf16 v[122:125], v[78:81], v[192:195], v[122:125]
	v_mfma_f32_16x16x32_bf16 v[110:113], v[70:73], v[216:219], v[110:113]
	v_mfma_f32_16x16x32_bf16 v[106:109], v[78:81], v[216:219], v[106:109]
	v_mfma_f32_16x16x32_bf16 v[94:97], v[70:73], v[224:227], v[94:97]
	v_mfma_f32_16x16x32_bf16 v[90:93], v[78:81], v[224:227], v[90:93]
	v_mfma_f32_16x16x32_bf16 v[134:137], v[146:149], v[180:183], v[134:137]
	v_mfma_f32_16x16x32_bf16 v[130:133], v[166:169], v[180:183], v[130:133]
	v_mfma_f32_16x16x32_bf16 v[118:121], v[146:149], v[188:191], v[118:121]
	v_mfma_f32_16x16x32_bf16 v[114:117], v[166:169], v[188:191], v[114:117]
	v_mfma_f32_16x16x32_bf16 v[102:105], v[146:149], v[212:215], v[102:105]
	v_mfma_f32_16x16x32_bf16 v[98:101], v[166:169], v[212:215], v[98:101]
	v_mfma_f32_16x16x32_bf16 v[86:89], v[146:149], v[220:223], v[86:89]
	v_mfma_f32_16x16x32_bf16 v[82:85], v[166:169], v[220:223], v[82:85]
	v_mfma_f32_16x16x32_bf16 v[134:137], v[150:153], v[184:187], v[134:137]
	v_mfma_f32_16x16x32_bf16 v[130:133], v[176:179], v[184:187], v[130:133]
	v_mfma_f32_16x16x32_bf16 v[118:121], v[150:153], v[192:195], v[118:121]
	v_mfma_f32_16x16x32_bf16 v[114:117], v[176:179], v[192:195], v[114:117]
	v_mfma_f32_16x16x32_bf16 v[102:105], v[150:153], v[216:219], v[102:105]
	v_mfma_f32_16x16x32_bf16 v[98:101], v[176:179], v[216:219], v[98:101]
	v_mfma_f32_16x16x32_bf16 v[86:89], v[150:153], v[224:227], v[86:89]
	v_mfma_f32_16x16x32_bf16 v[82:85], v[176:179], v[224:227], v[82:85]
	s_barrier
	s_mov_b32 m0, s31
	s_add_u32 s62, s4, 0x40000
	ds_read_b128 v[180:183], v175 offset:16384
	ds_read_b128 v[184:187], v175 offset:17408
	ds_read_b128 v[188:191], v175 offset:18432
	ds_read_b128 v[192:195], v175 offset:19456
	ds_read_b128 v[212:215], v175 offset:20480
	ds_read_b128 v[216:219], v175 offset:21504
	ds_read_b128 v[220:223], v175 offset:22528
	ds_read_b128 v[224:227], v175 offset:23552
	global_load_lds_dwordx4 v158, s[4:5]
	s_mov_b32 m0, s33
	s_addc_u32 s63, s5, 0
	global_load_lds_dwordx4 v154, s[4:5]
	s_mov_b32 m0, s35
	s_nop 0
	global_load_lds_dwordx4 v158, s[62:63]
	s_mov_b32 m0, s36
	s_nop 0
	global_load_lds_dwordx4 v154, s[62:63]
	s_mov_b32 m0, s37
	s_nop 0
	global_load_lds_dwordx4 v160, s[26:27]
	s_mov_b32 m0, s38
	s_nop 0
	global_load_lds_dwordx4 v156, s[26:27]
	s_waitcnt vmcnt(8)
	s_waitcnt lgkmcnt(0)
	s_barrier
	s_waitcnt lgkmcnt(0)
	v_mfma_f32_16x16x32_bf16 v[60:63], v[66:69], v[180:183], v[60:63]
	v_mfma_f32_16x16x32_bf16 v[56:59], v[74:77], v[180:183], v[56:59]
	v_mfma_f32_16x16x32_bf16 v[44:47], v[66:69], v[188:191], v[44:47]
	v_mfma_f32_16x16x32_bf16 v[40:43], v[74:77], v[188:191], v[40:43]
	v_mfma_f32_16x16x32_bf16 v[28:31], v[66:69], v[212:215], v[28:31]
	v_mfma_f32_16x16x32_bf16 v[24:27], v[74:77], v[212:215], v[24:27]
	v_mfma_f32_16x16x32_bf16 v[12:15], v[66:69], v[220:223], v[12:15]
	v_mfma_f32_16x16x32_bf16 v[8:11], v[74:77], v[220:223], v[8:11]
	v_mfma_f32_16x16x32_bf16 v[60:63], v[70:73], v[184:187], v[60:63]
	v_mfma_f32_16x16x32_bf16 v[56:59], v[78:81], v[184:187], v[56:59]
	v_mfma_f32_16x16x32_bf16 v[44:47], v[70:73], v[192:195], v[44:47]
	v_mfma_f32_16x16x32_bf16 v[40:43], v[78:81], v[192:195], v[40:43]
	v_mfma_f32_16x16x32_bf16 v[28:31], v[70:73], v[216:219], v[28:31]
	v_mfma_f32_16x16x32_bf16 v[24:27], v[78:81], v[216:219], v[24:27]
	v_mfma_f32_16x16x32_bf16 v[12:15], v[70:73], v[224:227], v[12:15]
	v_mfma_f32_16x16x32_bf16 v[8:11], v[78:81], v[224:227], v[8:11]
	v_mfma_f32_16x16x32_bf16 v[52:55], v[146:149], v[180:183], v[52:55]
	v_mfma_f32_16x16x32_bf16 v[48:51], v[166:169], v[180:183], v[48:51]
	v_mfma_f32_16x16x32_bf16 v[36:39], v[146:149], v[188:191], v[36:39]
	v_mfma_f32_16x16x32_bf16 v[32:35], v[166:169], v[188:191], v[32:35]
	v_mfma_f32_16x16x32_bf16 v[20:23], v[146:149], v[212:215], v[20:23]
	v_mfma_f32_16x16x32_bf16 v[16:19], v[166:169], v[212:215], v[16:19]
	v_mfma_f32_16x16x32_bf16 v[4:7], v[146:149], v[220:223], v[4:7]
	v_mfma_f32_16x16x32_bf16 v[0:3], v[166:169], v[220:223], v[0:3]
	v_mfma_f32_16x16x32_bf16 v[52:55], v[150:153], v[184:187], v[52:55]
	v_mfma_f32_16x16x32_bf16 v[48:51], v[176:179], v[184:187], v[48:51]
	v_mfma_f32_16x16x32_bf16 v[36:39], v[150:153], v[192:195], v[36:39]
	v_mfma_f32_16x16x32_bf16 v[32:35], v[176:179], v[192:195], v[32:35]
	v_mfma_f32_16x16x32_bf16 v[20:23], v[150:153], v[216:219], v[20:23]
	v_mfma_f32_16x16x32_bf16 v[16:19], v[176:179], v[216:219], v[16:19]
	v_mfma_f32_16x16x32_bf16 v[4:7], v[150:153], v[224:227], v[4:7]
	v_mfma_f32_16x16x32_bf16 v[0:3], v[176:179], v[224:227], v[0:3]
	s_barrier
	v_add_u32_e32 v64, s43, v173
	ds_read_b128 v[66:69], v64
	ds_read_b128 v[70:73], v64 offset:1024
	ds_read_b128 v[74:77], v64 offset:2048
	ds_read_b128 v[78:81], v64 offset:3072
	v_add_u32_e32 v64, s48, v173
	ds_read_b128 v[146:149], v64
	ds_read_b128 v[150:153], v64 offset:1024
	ds_read_b128 v[166:169], v64 offset:2048
	ds_read_b128 v[176:179], v64 offset:3072
	s_add_u32 s26, s26, 0x40000
	s_addc_u32 s27, s27, 0
	s_mov_b32 m0, s39
	ds_read_b128 v[180:183], v175 offset:32768
	ds_read_b128 v[184:187], v175 offset:33792
	ds_read_b128 v[188:191], v175 offset:34816
	ds_read_b128 v[192:195], v175 offset:35840
	ds_read_b128 v[212:215], v175 offset:36864
	ds_read_b128 v[216:219], v175 offset:37888
	ds_read_b128 v[220:223], v175 offset:38912
	ds_read_b128 v[224:227], v175 offset:39936
	global_load_lds_dwordx4 v160, s[26:27]
	s_mov_b32 m0, s40
	s_nop 0
	global_load_lds_dwordx4 v156, s[26:27]
	s_waitcnt vmcnt(8)
	s_waitcnt lgkmcnt(0)
	s_barrier
	s_waitcnt lgkmcnt(0)
	v_mfma_f32_16x16x32_bf16 v[142:145], v[66:69], v[180:183], v[142:145]
	v_mfma_f32_16x16x32_bf16 v[138:141], v[74:77], v[180:183], v[138:141]
	v_mfma_f32_16x16x32_bf16 v[126:129], v[66:69], v[188:191], v[126:129]
	v_mfma_f32_16x16x32_bf16 v[122:125], v[74:77], v[188:191], v[122:125]
	v_mfma_f32_16x16x32_bf16 v[110:113], v[66:69], v[212:215], v[110:113]
	v_mfma_f32_16x16x32_bf16 v[106:109], v[74:77], v[212:215], v[106:109]
	v_mfma_f32_16x16x32_bf16 v[94:97], v[66:69], v[220:223], v[94:97]
	v_mfma_f32_16x16x32_bf16 v[90:93], v[74:77], v[220:223], v[90:93]
	v_mfma_f32_16x16x32_bf16 v[142:145], v[70:73], v[184:187], v[142:145]
	v_mfma_f32_16x16x32_bf16 v[138:141], v[78:81], v[184:187], v[138:141]
	v_mfma_f32_16x16x32_bf16 v[126:129], v[70:73], v[192:195], v[126:129]
	v_mfma_f32_16x16x32_bf16 v[122:125], v[78:81], v[192:195], v[122:125]
	v_mfma_f32_16x16x32_bf16 v[110:113], v[70:73], v[216:219], v[110:113]
	v_mfma_f32_16x16x32_bf16 v[106:109], v[78:81], v[216:219], v[106:109]
	v_mfma_f32_16x16x32_bf16 v[94:97], v[70:73], v[224:227], v[94:97]
	v_mfma_f32_16x16x32_bf16 v[90:93], v[78:81], v[224:227], v[90:93]
	v_mfma_f32_16x16x32_bf16 v[134:137], v[146:149], v[180:183], v[134:137]
	v_mfma_f32_16x16x32_bf16 v[130:133], v[166:169], v[180:183], v[130:133]
	v_mfma_f32_16x16x32_bf16 v[118:121], v[146:149], v[188:191], v[118:121]
	v_mfma_f32_16x16x32_bf16 v[114:117], v[166:169], v[188:191], v[114:117]
	v_mfma_f32_16x16x32_bf16 v[102:105], v[146:149], v[212:215], v[102:105]
	v_mfma_f32_16x16x32_bf16 v[98:101], v[166:169], v[212:215], v[98:101]
	v_mfma_f32_16x16x32_bf16 v[86:89], v[146:149], v[220:223], v[86:89]
	v_mfma_f32_16x16x32_bf16 v[82:85], v[166:169], v[220:223], v[82:85]
	v_mfma_f32_16x16x32_bf16 v[134:137], v[150:153], v[184:187], v[134:137]
	v_mfma_f32_16x16x32_bf16 v[130:133], v[176:179], v[184:187], v[130:133]
	v_mfma_f32_16x16x32_bf16 v[118:121], v[150:153], v[192:195], v[118:121]
	v_mfma_f32_16x16x32_bf16 v[114:117], v[176:179], v[192:195], v[114:117]
	v_mfma_f32_16x16x32_bf16 v[102:105], v[150:153], v[216:219], v[102:105]
	v_mfma_f32_16x16x32_bf16 v[98:101], v[176:179], v[216:219], v[98:101]
	v_mfma_f32_16x16x32_bf16 v[86:89], v[150:153], v[224:227], v[86:89]
	v_mfma_f32_16x16x32_bf16 v[82:85], v[176:179], v[224:227], v[82:85]
	s_barrier
	s_mov_b32 m0, s44
	s_add_u32 s100, s4, s68
	s_addc_u32 s101, s5, s69
	s_add_u32 s4, s4, 0x40080
	ds_read_b128 v[180:183], v175 offset:49152
	ds_read_b128 v[184:187], v175 offset:50176
	ds_read_b128 v[188:191], v175 offset:51200
	ds_read_b128 v[192:195], v175 offset:52224
	ds_read_b128 v[212:215], v175 offset:53248
	ds_read_b128 v[216:219], v175 offset:54272
	ds_read_b128 v[220:223], v175 offset:55296
	ds_read_b128 v[224:227], v175 offset:56320
	global_load_lds_dwordx4 v158, s[100:101]
	s_mov_b32 m0, s45
	s_addc_u32 s5, s5, 0
	global_load_lds_dwordx4 v154, s[100:101]
	s_mov_b32 m0, s49
	s_add_u32 s100, s26, s68
	global_load_lds_dwordx4 v158, s[4:5]
	s_addc_u32 s101, s27, s69
	s_mov_b32 m0, s50
	s_sub_u32 s100, s100, 0x40000
	global_load_lds_dwordx4 v154, s[4:5]
	s_subb_u32 s101, s101, 0
	s_mov_b32 m0, s46
	s_nop 0
	global_load_lds_dwordx4 v160, s[100:101]
	s_mov_b32 m0, s47
	s_nop 0
	global_load_lds_dwordx4 v156, s[100:101]
	s_waitcnt vmcnt(8)
	s_waitcnt lgkmcnt(0)
	s_barrier
	s_waitcnt lgkmcnt(0)
	v_mfma_f32_16x16x32_bf16 v[60:63], v[66:69], v[180:183], v[60:63]
	v_mfma_f32_16x16x32_bf16 v[56:59], v[74:77], v[180:183], v[56:59]
	v_mfma_f32_16x16x32_bf16 v[44:47], v[66:69], v[188:191], v[44:47]
	v_mfma_f32_16x16x32_bf16 v[40:43], v[74:77], v[188:191], v[40:43]
	v_mfma_f32_16x16x32_bf16 v[28:31], v[66:69], v[212:215], v[28:31]
	v_mfma_f32_16x16x32_bf16 v[24:27], v[74:77], v[212:215], v[24:27]
	v_mfma_f32_16x16x32_bf16 v[12:15], v[66:69], v[220:223], v[12:15]
	v_mfma_f32_16x16x32_bf16 v[8:11], v[74:77], v[220:223], v[8:11]
	v_mfma_f32_16x16x32_bf16 v[60:63], v[70:73], v[184:187], v[60:63]
	v_mfma_f32_16x16x32_bf16 v[56:59], v[78:81], v[184:187], v[56:59]
	v_mfma_f32_16x16x32_bf16 v[44:47], v[70:73], v[192:195], v[44:47]
	v_mfma_f32_16x16x32_bf16 v[40:43], v[78:81], v[192:195], v[40:43]
	v_mfma_f32_16x16x32_bf16 v[28:31], v[70:73], v[216:219], v[28:31]
	v_mfma_f32_16x16x32_bf16 v[24:27], v[78:81], v[216:219], v[24:27]
	v_mfma_f32_16x16x32_bf16 v[12:15], v[70:73], v[224:227], v[12:15]
	v_mfma_f32_16x16x32_bf16 v[8:11], v[78:81], v[224:227], v[8:11]
	v_mfma_f32_16x16x32_bf16 v[52:55], v[146:149], v[180:183], v[52:55]
	v_mfma_f32_16x16x32_bf16 v[48:51], v[166:169], v[180:183], v[48:51]
	v_mfma_f32_16x16x32_bf16 v[36:39], v[146:149], v[188:191], v[36:39]
	v_mfma_f32_16x16x32_bf16 v[32:35], v[166:169], v[188:191], v[32:35]
	v_mfma_f32_16x16x32_bf16 v[20:23], v[146:149], v[212:215], v[20:23]
	v_mfma_f32_16x16x32_bf16 v[16:19], v[166:169], v[212:215], v[16:19]
	v_mfma_f32_16x16x32_bf16 v[4:7], v[146:149], v[220:223], v[4:7]
	v_mfma_f32_16x16x32_bf16 v[0:3], v[166:169], v[220:223], v[0:3]
	v_mfma_f32_16x16x32_bf16 v[52:55], v[150:153], v[184:187], v[52:55]
	v_mfma_f32_16x16x32_bf16 v[48:51], v[176:179], v[184:187], v[48:51]
	v_mfma_f32_16x16x32_bf16 v[36:39], v[150:153], v[192:195], v[36:39]
	v_mfma_f32_16x16x32_bf16 v[32:35], v[176:179], v[192:195], v[32:35]
	v_mfma_f32_16x16x32_bf16 v[20:23], v[150:153], v[216:219], v[20:23]
	v_mfma_f32_16x16x32_bf16 v[16:19], v[176:179], v[216:219], v[16:19]
	v_mfma_f32_16x16x32_bf16 v[4:7], v[150:153], v[224:227], v[4:7]
	v_mfma_f32_16x16x32_bf16 v[0:3], v[176:179], v[224:227], v[0:3]
	s_add_i32 s61, s61, 2
	s_add_u32 s0, s0, 0x100
	s_addc_u32 s1, s1, 0
	s_add_u32 s59, s59, 0x100
	s_addc_u32 s60, s60, 0
	s_cmp_gt_u32 s61, 13
	s_barrier
	s_cbranch_scc0 .LBB0_814
	s_and_b64 vcc, exec, s[20:21]
	s_cbranch_vccz .LBB0_817
	s_barrier
